# B1'': last XCD leader bumps the 16 per-XCC release words before TOPGEN (the 248 waiting workgroups are released ahead of the 7 other leaders); on top of A8 stack
# baseline (speedup 1.0000x reference)
.LBB0_194:
	s_or_b64 exec, exec, s[6:7]
	s_and_saveexec_b64 s[2:3], s[10:11]
	s_cbranch_execz .LBB0_196
	v_mov_b32_e32 v2, 1
	global_atomic_add v[0:1], v2, off offset:128
	global_atomic_add v[0:1], v2, off offset:256
	global_atomic_add v[0:1], v2, off offset:384
	global_atomic_add v[0:1], v2, off offset:512
	global_atomic_add v[0:1], v2, off offset:640
	global_atomic_add v[0:1], v2, off offset:768
	global_atomic_add v[0:1], v2, off offset:896
	global_atomic_add v[0:1], v2, off offset:1024
	global_atomic_add v[0:1], v2, off offset:1152
	global_atomic_add v[0:1], v2, off offset:1280
	global_atomic_add v[0:1], v2, off offset:1408
	global_atomic_add v[0:1], v2, off offset:1536
	global_atomic_add v[0:1], v2, off offset:1664
	global_atomic_add v[0:1], v2, off offset:1792
	global_atomic_add v[0:1], v2, off offset:1920
	global_atomic_add v[0:1], v2, off offset:2048
	global_atomic_add v[0:1], v2, off

.LBB0_249:
	s_or_b64 exec, exec, s[6:7]
	s_and_saveexec_b64 s[0:1], s[10:11]
	s_cbranch_execz .LBB0_251
	v_mov_b32_e32 v2, 1
	global_atomic_add v[0:1], v2, off offset:128
	global_atomic_add v[0:1], v2, off offset:256
	global_atomic_add v[0:1], v2, off offset:384
	global_atomic_add v[0:1], v2, off offset:512
	global_atomic_add v[0:1], v2, off offset:640
	global_atomic_add v[0:1], v2, off offset:768
	global_atomic_add v[0:1], v2, off offset:896
	global_atomic_add v[0:1], v2, off offset:1024
	global_atomic_add v[0:1], v2, off offset:1152
	global_atomic_add v[0:1], v2, off offset:1280
	global_atomic_add v[0:1], v2, off offset:1408
	global_atomic_add v[0:1], v2, off offset:1536
	global_atomic_add v[0:1], v2, off offset:1664
	global_atomic_add v[0:1], v2, off offset:1792
	global_atomic_add v[0:1], v2, off offset:1920
	global_atomic_add v[0:1], v2, off offset:2048
	global_atomic_add v[0:1], v2, off

.LBB0_321:
	s_or_b64 exec, exec, s[8:9]
	s_and_saveexec_b64 s[2:3], s[10:11]
	s_cbranch_execz .LBB0_323
	global_atomic_add v[0:1], v190, off offset:128
	global_atomic_add v[0:1], v190, off offset:256
	global_atomic_add v[0:1], v190, off offset:384
	global_atomic_add v[0:1], v190, off offset:512
	global_atomic_add v[0:1], v190, off offset:640
	global_atomic_add v[0:1], v190, off offset:768
	global_atomic_add v[0:1], v190, off offset:896
	global_atomic_add v[0:1], v190, off offset:1024
	global_atomic_add v[0:1], v190, off offset:1152
	global_atomic_add v[0:1], v190, off offset:1280
	global_atomic_add v[0:1], v190, off offset:1408
	global_atomic_add v[0:1], v190, off offset:1536
	global_atomic_add v[0:1], v190, off offset:1664
	global_atomic_add v[0:1], v190, off offset:1792
	global_atomic_add v[0:1], v190, off offset:1920
	global_atomic_add v[0:1], v190, off offset:2048
	global_atomic_add v[0:1], v190, off
